# prologue x conversion (A', bf16 x, row sums): 16 loads of a row in flight together instead of 8 serialised chunks
# baseline (speedup 1.0000x reference)
; __device__ __forceinline__ unsigned cvt_pk_bf16(float lo, float hi) { const f32x2_t v = {lo, hi}; const bf16x2_t b = __builtin_convertvector(v, bf16x2_t); return __builtin_bit_cast(unsigned, b); }
; __global__ void __launch_bounds__(NWAVES * 64, 2) mk_fwd(Args args) {
;     ...
;     for (int t = gw; t < T; t += NGW) {
;         float ssq = 0.f;
; #pragma unroll
;         for (int c = lane * 4; c < D; c += 256) { const f32x4 v = *(const f32x4*)(x_in + (size_t)t * D + c); const f32x4 g = *(const f32x4*)(W_gs + c);
;             ssq += (v[0] * v[0] + v[1] * v[1]) + (v[2] * v[2] + v[3] * v[3]);
;             u32x2 o; o.x = pg8::cvt_pk_bf16(v[0] * g[0], v[1] * g[1]); o.y = pg8::cvt_pk_bf16(v[2] * g[2], v[3] * g[3]); *(u32x2*)(W_ap + ((size_t)((t >> 8) * (D / 64) + (c >> 6)) * 256 + (t & 255)) * 64 + (c & 63)) = o;
;             u32x2 xo; xo.x = pg8::cvt_pk_bf16(v[0], v[1]); xo.y = pg8::cvt_pk_bf16(v[2], v[3]); *(u32x2*)(W_x + XIDX(t, c)) = xo; }
.LBB0_137:
	v_add_co_u32_e32 v46, vcc, 0xfffff000, v30
	s_ashr_i32 s9, s12, 3
	s_nop 0
	v_addc_co_u32_e32 v47, vcc, -1, v31, vcc
	s_andn2_b32 s9, s9, 31
	s_lshl_b32 s8, s10, 1
	s_and_b32 s8, s8, 0x7f80
	s_waitcnt lgkmcnt(0)
	global_load_dwordx4 v[146:149], v[46:47], off offset:-3072
	global_load_dwordx4 v[150:153], v[46:47], off offset:-2048
	global_load_dwordx4 v[154:157], v[46:47], off offset:-1024
	global_load_dwordx4 v[158:161], v[30:31], off offset:-4096
	global_load_dwordx4 v[162:165], v[30:31], off offset:-3072
	global_load_dwordx4 v[166:169], v[30:31], off offset:-2048
	global_load_dwordx4 v[170:173], v[30:31], off offset:-1024
	global_load_dwordx4 v[174:177], v[30:31], off
	global_load_dwordx4 v[178:181], v[8:9], off
	global_load_dwordx4 v[182:185], v[14:15], off
	global_load_dwordx4 v[186:189], v[16:17], off
	global_load_dwordx4 v[190:193], v[18:19], off
	global_load_dwordx4 v[194:197], v[20:21], off
	global_load_dwordx4 v[198:201], v[22:23], off
	global_load_dwordx4 v[202:205], v[24:25], off
	global_load_dwordx4 v[206:209], v[26:27], off
	s_waitcnt vmcnt(0)
; __device__ __forceinline__ unsigned cvt_pk_bf16(float lo, float hi) { const f32x2_t v = {lo, hi}; const bf16x2_t b = __builtin_convertvector(v, bf16x2_t); return __builtin_bit_cast(unsigned, b); }
; __global__ void __launch_bounds__(NWAVES * 64, 2) mk_fwd(Args args) {
;     ...
;     for (int t = gw; t < T; t += NGW) {
;         float ssq = 0.f;
; #pragma unroll
;         for (int c = lane * 4; c < D; c += 256) { const f32x4 v = *(const f32x4*)(x_in + (size_t)t * D + c); const f32x4 g = *(const f32x4*)(W_gs + c);
;             ssq += (v[0] * v[0] + v[1] * v[1]) + (v[2] * v[2] + v[3] * v[3]);
;             u32x2 o; o.x = pg8::cvt_pk_bf16(v[0] * g[0], v[1] * g[1]); o.y = pg8::cvt_pk_bf16(v[2] * g[2], v[3] * g[3]); *(u32x2*)(W_ap + ((size_t)((t >> 8) * (D / 64) + (c >> 6)) * 256 + (t & 255)) * 64 + (c & 63)) = o;
;             u32x2 xo; xo.x = pg8::cvt_pk_bf16(v[0], v[1]); xo.y = pg8::cvt_pk_bf16(v[2], v[3]); *(u32x2*)(W_x + XIDX(t, c)) = xo; }
;         ssq = wave_sum(ssq);
;         if (lane < 32) W_ss[(size_t)t * 32 + lane] = lane == 0 ? ssq : 0.f;
	v_or_b32_e32 v50, s9, v39
	v_ashrrev_i32_e32 v51, 31, v50
	v_lshlrev_b64 v[50:51], 15, v[50:51]
	v_or_b32_e32 v50, s8, v50
	v_lshl_add_u64 v[52:53], v[10:11], 0, v[50:51]
	v_lshl_add_u64 v[50:51], v[12:13], 0, v[50:51]
	v_pk_mul_f32 v[6:7], v[148:149], v[180:181]
	v_pk_mul_f32 v[4:5], v[146:147], v[178:179]
	v_cvt_pk_bf16_f32 v54, v146, v147
	v_cvt_pk_bf16_f32 v55, v148, v149
	v_cvt_pk_bf16_f32 v4, v4, v5
	v_cvt_pk_bf16_f32 v5, v6, v7
	global_store_dwordx2 v[50:51], v[54:55], off
	global_store_dwordx2 v[52:53], v[4:5], off
	v_mul_f32_e32 v1, v147, v147
	v_mul_f32_e32 v3, v149, v149
	v_fmac_f32_e32 v1, v146, v146
	v_fmac_f32_e32 v3, v148, v148
	v_add_f32_e32 v0, v1, v3
	v_or_b32_e32 v50, s9, v40
	v_ashrrev_i32_e32 v51, 31, v50
	v_lshlrev_b64 v[50:51], 15, v[50:51]
	v_or_b32_e32 v50, s8, v50
	v_lshl_add_u64 v[52:53], v[10:11], 0, v[50:51]
	v_lshl_add_u64 v[50:51], v[12:13], 0, v[50:51]
	v_pk_mul_f32 v[6:7], v[152:153], v[184:185]
	v_pk_mul_f32 v[4:5], v[150:151], v[182:183]
	v_cvt_pk_bf16_f32 v54, v150, v151
	v_cvt_pk_bf16_f32 v55, v152, v153
	v_cvt_pk_bf16_f32 v4, v4, v5
	v_cvt_pk_bf16_f32 v5, v6, v7
	global_store_dwordx2 v[50:51], v[54:55], off
	global_store_dwordx2 v[52:53], v[4:5], off
	v_mul_f32_e32 v1, v151, v151
	v_mul_f32_e32 v2, v153, v153
	v_fmac_f32_e32 v1, v150, v150
	v_fmac_f32_e32 v2, v152, v152
	v_add_f32_e32 v1, v1, v2
	v_add_f32_e32 v0, v0, v1
	v_or_b32_e32 v50, s9, v41
	v_ashrrev_i32_e32 v51, 31, v50
	v_lshlrev_b64 v[50:51], 15, v[50:51]
	v_or_b32_e32 v50, s8, v50
	v_lshl_add_u64 v[52:53], v[10:11], 0, v[50:51]
	v_lshl_add_u64 v[50:51], v[12:13], 0, v[50:51]
	v_pk_mul_f32 v[6:7], v[156:157], v[188:189]
	v_pk_mul_f32 v[4:5], v[154:155], v[186:187]
	v_cvt_pk_bf16_f32 v54, v154, v155
	v_cvt_pk_bf16_f32 v55, v156, v157
	v_cvt_pk_bf16_f32 v4, v4, v5
	v_cvt_pk_bf16_f32 v5, v6, v7
	global_store_dwordx2 v[50:51], v[54:55], off
	global_store_dwordx2 v[52:53], v[4:5], off
	v_mul_f32_e32 v1, v155, v155
	v_mul_f32_e32 v2, v157, v157
	v_fmac_f32_e32 v1, v154, v154
	v_fmac_f32_e32 v2, v156, v156
	v_add_f32_e32 v1, v1, v2
	v_add_f32_e32 v0, v0, v1
	v_or_b32_e32 v50, s9, v42
	v_ashrrev_i32_e32 v51, 31, v50
	v_lshlrev_b64 v[50:51], 15, v[50:51]
	v_or_b32_e32 v50, s8, v50
	v_lshl_add_u64 v[52:53], v[10:11], 0, v[50:51]
	v_lshl_add_u64 v[50:51], v[12:13], 0, v[50:51]
	v_pk_mul_f32 v[6:7], v[160:161], v[192:193]
	v_pk_mul_f32 v[4:5], v[158:159], v[190:191]
	v_cvt_pk_bf16_f32 v54, v158, v159
	v_cvt_pk_bf16_f32 v55, v160, v161
	v_cvt_pk_bf16_f32 v4, v4, v5
	v_cvt_pk_bf16_f32 v5, v6, v7
	global_store_dwordx2 v[50:51], v[54:55], off
	global_store_dwordx2 v[52:53], v[4:5], off
	v_mul_f32_e32 v1, v159, v159
	v_mul_f32_e32 v2, v161, v161
	v_fmac_f32_e32 v1, v158, v158
	v_fmac_f32_e32 v2, v160, v160
	v_add_f32_e32 v1, v1, v2
	v_add_f32_e32 v0, v0, v1
	v_or_b32_e32 v50, s9, v43
	v_ashrrev_i32_e32 v51, 31, v50
	v_lshlrev_b64 v[50:51], 15, v[50:51]
	v_or_b32_e32 v50, s8, v50
	v_lshl_add_u64 v[52:53], v[10:11], 0, v[50:51]
	v_lshl_add_u64 v[50:51], v[12:13], 0, v[50:51]
	v_pk_mul_f32 v[6:7], v[164:165], v[196:197]
	v_pk_mul_f32 v[4:5], v[162:163], v[194:195]
	v_cvt_pk_bf16_f32 v54, v162, v163
	v_cvt_pk_bf16_f32 v55, v164, v165
	v_cvt_pk_bf16_f32 v4, v4, v5
	v_cvt_pk_bf16_f32 v5, v6, v7
	global_store_dwordx2 v[50:51], v[54:55], off
	global_store_dwordx2 v[52:53], v[4:5], off
	v_mul_f32_e32 v1, v163, v163
	v_mul_f32_e32 v2, v165, v165
	v_fmac_f32_e32 v1, v162, v162
	v_fmac_f32_e32 v2, v164, v164
	v_add_f32_e32 v1, v1, v2
	v_add_f32_e32 v0, v0, v1
	v_or_b32_e32 v50, s9, v44
	v_ashrrev_i32_e32 v51, 31, v50
	v_lshlrev_b64 v[50:51], 15, v[50:51]
	v_or_b32_e32 v50, s8, v50
	v_lshl_add_u64 v[52:53], v[10:11], 0, v[50:51]
	v_lshl_add_u64 v[50:51], v[12:13], 0, v[50:51]
	v_pk_mul_f32 v[6:7], v[168:169], v[200:201]
	v_pk_mul_f32 v[4:5], v[166:167], v[198:199]
	v_cvt_pk_bf16_f32 v54, v166, v167
	v_cvt_pk_bf16_f32 v55, v168, v169
	v_cvt_pk_bf16_f32 v4, v4, v5
	v_cvt_pk_bf16_f32 v5, v6, v7
	global_store_dwordx2 v[50:51], v[54:55], off
	global_store_dwordx2 v[52:53], v[4:5], off
	v_mul_f32_e32 v1, v167, v167
	v_mul_f32_e32 v2, v169, v169
	v_fmac_f32_e32 v1, v166, v166
	v_fmac_f32_e32 v2, v168, v168
	v_add_f32_e32 v1, v1, v2
	v_add_f32_e32 v0, v0, v1
	v_or_b32_e32 v50, s9, v45
	v_ashrrev_i32_e32 v51, 31, v50
	v_lshlrev_b64 v[50:51], 15, v[50:51]
	v_or_b32_e32 v50, s8, v50
	v_lshl_add_u64 v[52:53], v[10:11], 0, v[50:51]
	v_lshl_add_u64 v[50:51], v[12:13], 0, v[50:51]
	v_pk_mul_f32 v[6:7], v[172:173], v[204:205]
	v_pk_mul_f32 v[4:5], v[170:171], v[202:203]
	v_cvt_pk_bf16_f32 v54, v170, v171
	v_cvt_pk_bf16_f32 v55, v172, v173
	v_cvt_pk_bf16_f32 v4, v4, v5
	v_cvt_pk_bf16_f32 v5, v6, v7
	global_store_dwordx2 v[50:51], v[54:55], off
	global_store_dwordx2 v[52:53], v[4:5], off
	v_mul_f32_e32 v1, v171, v171
	v_mul_f32_e32 v2, v173, v173
	v_fmac_f32_e32 v1, v170, v170
	v_fmac_f32_e32 v2, v172, v172
	v_add_f32_e32 v1, v1, v2
	v_add_f32_e32 v0, v0, v1
	v_or_b32_e32 v50, s9, v48
	v_ashrrev_i32_e32 v51, 31, v50
	v_lshlrev_b64 v[50:51], 15, v[50:51]
	v_or_b32_e32 v50, s8, v50
	v_lshl_add_u64 v[52:53], v[10:11], 0, v[50:51]
	v_lshl_add_u64 v[50:51], v[12:13], 0, v[50:51]
	v_pk_mul_f32 v[6:7], v[176:177], v[208:209]
	v_pk_mul_f32 v[4:5], v[174:175], v[206:207]
	v_cvt_pk_bf16_f32 v54, v174, v175
	v_cvt_pk_bf16_f32 v55, v176, v177
	v_cvt_pk_bf16_f32 v4, v4, v5
	v_cvt_pk_bf16_f32 v5, v6, v7
	global_store_dwordx2 v[50:51], v[54:55], off
	global_store_dwordx2 v[52:53], v[4:5], off
	v_mul_f32_e32 v1, v175, v175
	v_mul_f32_e32 v2, v177, v177
	v_fmac_f32_e32 v1, v174, v174
	v_fmac_f32_e32 v2, v176, v176
	v_add_f32_e32 v1, v1, v2
	v_add_f32_e32 v0, v0, v1
	ds_bpermute_b32 v1, v33, v0
	s_waitcnt lgkmcnt(0)
	v_add_f32_e32 v0, v0, v1
	ds_bpermute_b32 v1, v34, v0
	s_waitcnt lgkmcnt(0)
	v_add_f32_e32 v4, v0, v1
	ds_bpermute_b32 v5, v35, v4
	s_waitcnt lgkmcnt(0)
	v_add_f32_e32 v4, v4, v5
	ds_bpermute_b32 v5, v36, v4
	s_waitcnt lgkmcnt(0)
	v_add_f32_e32 v6, v4, v5
	ds_bpermute_b32 v7, v37, v6
	s_waitcnt lgkmcnt(0)
	v_add_f32_e32 v0, v6, v7
	ds_bpermute_b32 v1, v38, v0
	s_and_saveexec_b64 s[8:9], s[4:5]
	s_cbranch_execz .LBB0_136
	s_waitcnt lgkmcnt(0)
	v_add_f32_e32 v0, v0, v1
	v_cndmask_b32_e64 v0, 0, v0, s[2:3]
	global_store_dword v[28:29], v0, off
	s_branch .LBB0_136
